# speedup vs baseline: 1.0459x; 1.0459x over previous
.LBB5_15:
	s_or_b64 exec, exec, s[6:7]
	s_load_dwordx4 s[4:7], s[0:1], 0x18
	v_mov_b32_e32 v17, 0
	s_waitcnt lgkmcnt(0)
	s_barrier
	ds_read_b32 v17, v17 offset:32776
	s_and_b32 s17, s5, 0xffff
	s_and_b32 s21, s15, 0xffff
	v_accvgpr_read_b32 v56, a0
	v_lshlrev_b32_e32 v15, 12, v1
	v_lshlrev_b32_e32 v18, 4, v56
	s_add_u32 s8, s4, s7
	s_mov_b32 s16, s4
	v_lshlrev_b32_e32 v14, 14, v10
	v_lshlrev_b32_e32 v16, 7, v0
	s_addc_u32 s9, s5, 0
	s_waitcnt lgkmcnt(0)
	v_cmp_ne_u32_e64 s[4:5], 0, v17
	v_add_u32_e32 v17, 0, v15
	v_or_b32_e32 v15, v18, v15
	v_or3_b32 v15, v16, v14, v15
	v_lshlrev_b32_e32 v13, 3, v0
	v_accvgpr_write_b32 a98, v15
	v_and_b32_e32 v15, 63, v57
	v_lshlrev_b32_e32 v19, 4, v13
	v_lshrrev_b32_e32 v15, 5, v15
	s_waitcnt vmcnt(1)
	v_mul_f32_e32 v45, 0xbfb8aa3b, v6
	v_mul_f32_e32 v6, 0xbfb8aa3b, v7
	v_mul_f32_e32 v7, 0xbfb8aa3b, v9
	v_lshlrev_b32_e32 v9, 8, v1
	v_add3_u32 v17, v17, v19, v18
	v_accvgpr_write_b32 a94, v15
	v_bfe_u32 v16, v57, 2, 3
	v_lshlrev_b32_e32 v15, 3, v57
	v_add_u32_e32 v9, v23, v9
	v_accvgpr_write_b32 a97, v17
	v_and_b32_e32 v17, 24, v15
	v_lshlrev_b32_e32 v10, 13, v10
	v_lshlrev_b32_e32 v15, 10, v16
	v_or_b32_e32 v9, v9, v13
	v_or3_b32 v10, v10, v15, v17
	v_cmp_eq_u32_e64 s[2:3], 3, v1
	v_lshl_add_u32 v9, v9, 1, s6
	v_accvgpr_write_b32 a95, v16
	v_lshl_add_u32 v16, v10, 1, s44
	v_lshlrev_b32_e32 v1, 7, v1
	v_and_b32_e32 v10, 8, v57
	v_lshlrev_b32_e32 v0, 1, v0
	v_or3_b32 v1, v1, v10, v0
	v_add_u32_e32 v10, s24, v9
	s_lshl_b32 s6, s33, 9
	v_or3_b32 v1, v1, v18, v14
	v_accvgpr_write_b32 a99, v10
	v_add_u32_e32 v10, s26, v9
	v_add_u32_e32 v1, s6, v1
	s_and_b32 s33, s6, 0xe00
	s_lshl_b32 s6, s42, 9
	v_accvgpr_write_b32 a102, v10
	v_add_u32_e32 v10, s28, v9
	s_and_b32 s35, s6, 0xe00
	s_lshl_b32 s6, s43, 9
	v_accvgpr_write_b32 a103, v10
	v_add_u32_e32 v10, s30, v9
	s_and_b32 s37, s6, 0xe00
	s_lshl_b32 s6, s45, 9
	v_accvgpr_write_b32 a104, v10
	v_add_u32_e32 v10, s34, v9
	v_accvgpr_write_b32 a96, v17
	v_ashrrev_i32_e32 v17, 31, v16
	s_and_b32 s39, s6, 0xe00
	s_lshl_b32 s6, s46, 9
	v_accvgpr_write_b32 a105, v10
	v_add_u32_e32 v10, s36, v9
	v_accvgpr_write_b32 a93, v17
	s_and_b32 s41, s6, 0xe00
	s_lshl_b32 s6, s47, 9
	v_accvgpr_write_b32 a106, v10
	v_add_u32_e32 v10, s38, v9
	v_add_u32_e32 v9, s40, v9
	v_or_b32_e32 v13, v13, v56
	v_accvgpr_write_b32 a92, v16
	v_lshl_add_u64 v[16:17], s[8:9], 0, v[16:17]
	s_and_b32 s42, s6, 0xe00
	s_lshl_b32 s6, s48, 9
	v_accvgpr_write_b32 a108, v9
	v_lshlrev_b32_e32 v9, 1, v12
	s_mov_b32 s19, 0x20000
	v_accvgpr_write_b32 a101, v17
	s_and_b32 s43, s6, 0xe00
	s_lshl_b32 s6, s49, 9
	v_accvgpr_write_b32 a107, v10
	v_add3_u32 v0, 0, v9, v0
	v_lshlrev_b32_e32 v9, 9, v11
	v_lshlrev_b32_e32 v10, 4, v13
	s_brev_b32 s18, -2
	s_mov_b32 s22, 0x80000
	s_mov_b32 s23, s19
	s_mov_b32 s20, s14
	v_cmp_gt_u32_e64 s[0:1], 8, v22
	s_mov_b32 s15, 0
	v_accvgpr_write_b32 a100, v16
	s_and_b32 s44, s6, 0xe00
	v_add3_u32 v9, 0, v9, v10
	s_mov_b64 s[26:27], 0
	s_mov_b32 s34, 0x80008000
	s_mov_b32 s36, 0x100000
	s_brev_b32 s38, 60
	s_mov_b32 s40, 0xbc38aa3b
	s_mov_b32 s45, 0x41000000
	s_waitcnt vmcnt(0)
	v_accvgpr_write_b32 a112, v250
	v_accvgpr_write_b32 a113, v251
	v_accvgpr_write_b32 a114, v252
	v_accvgpr_write_b32 a115, v253
	v_accvgpr_write_b32 a116, v2
	v_accvgpr_write_b32 a117, v3
	v_accvgpr_write_b32 a118, v4
	v_accvgpr_write_b32 a119, v5
	v_and_b32_e32 v46, 8, v57
	v_cmp_ne_u32_e64 s[0:1], 0, v46
	v_and_b32_e32 v46, 32, v57
	v_cmp_ne_u32_e64 s[30:31], 0, v46
	v_mov_b32_e32 v26, 0x44444444
	v_mov_b32_e32 v46, 0xeeeeeeee
	v_cndmask_b32_e64 v26, v26, v46, s[0:1]
	v_accvgpr_read_b32 v46, a98
	v_bfe_u32 v47, v57, 4, 2
	v_lshlrev_b32_e32 v47, 7, v47
	v_sub_u32_e32 v46, v46, v47
	v_bfe_u32 v47, v57, 4, 1
	v_bfe_u32 v48, v57, 3, 1
	v_lshl_or_b32 v47, v47, 1, v48
	v_lshl_add_u32 v46, v47, 7, v46
	v_mov_b32_e32 v47, s33
	v_mov_b32_e32 v48, s35
	v_cndmask_b32_e64 v47, v47, v48, s[30:31]
	v_or_b32_e32 v27, v46, v47
	v_mov_b32_e32 v47, s37
	v_mov_b32_e32 v48, s39
	v_cndmask_b32_e64 v47, v47, v48, s[30:31]
	v_or_b32_e32 v28, v46, v47
	v_mov_b32_e32 v47, s41
	v_mov_b32_e32 v48, s42
	v_cndmask_b32_e64 v47, v47, v48, s[30:31]
	v_or_b32_e32 v29, v46, v47
	v_mov_b32_e32 v47, s43
	v_mov_b32_e32 v48, s44
	v_cndmask_b32_e64 v47, v47, v48, s[30:31]
	v_or_b32_e32 v30, v46, v47
	v_lshrrev_b32_e32 v46, 6, v57
	v_lshlrev_b32_e32 v46, 7, v46
	v_and_b32_e32 v47, 8, v57
	v_bfe_u32 v48, v57, 4, 2
	v_lshl_or_b32 v47, v48, 1, v47
	v_add_u32_e32 v46, v46, v47
	v_sub_u32_e32 v1, v1, v46
	v_bfe_u32 v46, v57, 7, 1
	v_bfe_u32 v47, v57, 5, 1
	v_lshl_or_b32 v46, v46, 1, v47
	v_lshlrev_b32_e32 v46, 7, v46
	v_bfe_u32 v47, v57, 3, 1
	v_bfe_u32 v48, v57, 6, 1
	v_lshl_or_b32 v47, v48, 1, v47
	v_lshl_or_b32 v46, v47, 2, v46
	v_bfe_u32 v47, v57, 4, 1
	v_lshl_or_b32 v46, v47, 1, v46
	v_add_u32_e32 v1, v1, v46
	v_lshrrev_b32_e32 v46, 4, v57
	v_lshlrev_b32_e32 v46, 11, v46
	v_and_b32_e32 v47, 3, v57
	v_lshl_or_b32 v46, v47, 2, v46
	v_and_b32_e32 v47, 16, v57
	v_lshl_or_b32 v46, v47, 3, v46
	v_bfe_u32 v47, v57, 2, 2
	v_xor_b32_e32 v48, 0, v47
	v_lshl_or_b32 v48, v48, 4, v46
	v_add_u32_e32 v31, 0, v48
	v_xor_b32_e32 v35, 0x80, v31
	v_xor_b32_e32 v48, 1, v47
	v_lshl_or_b32 v48, v48, 4, v46
	v_add_u32_e32 v32, 512, v48
	v_xor_b32_e32 v36, 0x80, v32
	v_xor_b32_e32 v48, 2, v47
	v_lshl_or_b32 v48, v48, 4, v46
	v_add_u32_e32 v33, 1024, v48
	v_xor_b32_e32 v37, 0x80, v33
	v_xor_b32_e32 v48, 3, v47
	v_lshl_or_b32 v48, v48, 4, v46
	v_add_u32_e32 v34, 1536, v48
	v_xor_b32_e32 v38, 0x80, v34
	v_lshrrev_b32_e32 v46, 3, v57
	v_and_b32_e32 v46, 24, v46
	v_lshrrev_b32_e32 v47, 1, v57
	v_and_or_b32 v46, v47, 4, v46
	v_bfe_u32 v47, v57, 4, 2
	v_or_b32_e32 v46, v46, v47
	v_and_b32_e32 v47, 3, v57
	v_and_b32_e32 v48, 4, v57
	v_lshl_or_b32 v47, v48, 1, v47
	v_xor_b32_e32 v46, v46, v47
	v_and_b32_e32 v47, 7, v57
	v_lshlrev_b32_e32 v47, 9, v47
	v_lshl_or_b32 v9, v46, 4, v47
	v_accvgpr_write_b32 a120, v226
	v_accvgpr_write_b32 a121, v227
	v_accvgpr_write_b32 a122, v228
	v_accvgpr_write_b32 a123, v229
	v_accvgpr_write_b32 a124, v230
	v_accvgpr_write_b32 a125, v231
	v_accvgpr_write_b32 a126, v232
	v_accvgpr_write_b32 a127, v233
	v_accvgpr_write_b32 a128, v234
	v_accvgpr_write_b32 a129, v235
	v_accvgpr_write_b32 a130, v236
	v_accvgpr_write_b32 a131, v237
	v_accvgpr_write_b32 a132, v238
	v_accvgpr_write_b32 a133, v239
	v_accvgpr_write_b32 a134, v240
	v_accvgpr_write_b32 a135, v241
	v_accvgpr_write_b32 a136, v242
	v_accvgpr_write_b32 a137, v243
	v_accvgpr_write_b32 a138, v244
	v_accvgpr_write_b32 a139, v245
	v_accvgpr_write_b32 a140, v246
	v_accvgpr_write_b32 a141, v247
	v_accvgpr_write_b32 a142, v248
	v_accvgpr_write_b32 a143, v249
	s_mov_b64 s[24:25], 0
	s_mov_b32 s46, 0
	s_mov_b32 s30, 0x3c38aa3b
	s_mov_b32 s31, 0xbc000000
	v_accvgpr_write_b32 a0, 0
	v_accvgpr_write_b32 a1, 0
	v_accvgpr_write_b32 a2, 0
	v_accvgpr_write_b32 a3, 0
	v_accvgpr_write_b32 a4, 0
	v_accvgpr_write_b32 a5, 0
	v_accvgpr_write_b32 a6, 0
	v_accvgpr_write_b32 a7, 0
	v_accvgpr_write_b32 a8, 0
	v_accvgpr_write_b32 a9, 0
	v_accvgpr_write_b32 a10, 0
	v_accvgpr_write_b32 a11, 0
	v_accvgpr_write_b32 a12, 0
	v_accvgpr_write_b32 a13, 0
	v_accvgpr_write_b32 a14, 0
	v_accvgpr_write_b32 a15, 0
	v_accvgpr_write_b32 a16, 0
	v_accvgpr_write_b32 a17, 0
	v_accvgpr_write_b32 a18, 0
	v_accvgpr_write_b32 a19, 0
	v_accvgpr_write_b32 a20, 0
	v_accvgpr_write_b32 a21, 0
	v_accvgpr_write_b32 a22, 0
	v_accvgpr_write_b32 a23, 0
	v_accvgpr_write_b32 a24, 0
	v_accvgpr_write_b32 a25, 0
	v_accvgpr_write_b32 a26, 0
	v_accvgpr_write_b32 a27, 0
	v_accvgpr_write_b32 a28, 0
	v_accvgpr_write_b32 a29, 0
	v_accvgpr_write_b32 a30, 0
	v_accvgpr_write_b32 a31, 0
	v_bfe_u32 v50, v57, 4, 2
	v_lshlrev_b32_e32 v50, 4, v50
	v_bfe_u32 v51, v57, 4, 1
	v_bfe_u32 v52, v57, 3, 1
	v_lshlrev_b32_e32 v52, 2, v52
	v_lshl_or_b32 v51, v51, 5, v52
	v_sub_u32_e32 v50, v51, v50
	v_and_b32_e32 v46, 32, v57
	v_cmp_ne_u32_e64 s[28:29], 0, v46
	v_accvgpr_read_b32 v242, a99
	v_accvgpr_read_b32 v51, a102
	v_cndmask_b32_e64 v242, v242, v51, s[28:29]
	v_add_u32_e32 v242, v242, v50
	v_accvgpr_read_b32 v243, a103
	v_accvgpr_read_b32 v51, a104
	v_cndmask_b32_e64 v243, v243, v51, s[28:29]
	v_add_u32_e32 v243, v243, v50
	v_accvgpr_read_b32 v244, a105
	v_accvgpr_read_b32 v51, a106
	v_cndmask_b32_e64 v244, v244, v51, s[28:29]
	v_add_u32_e32 v244, v244, v50
	v_accvgpr_read_b32 v245, a107
	v_accvgpr_read_b32 v51, a108
	v_cndmask_b32_e64 v245, v245, v51, s[28:29]
	v_add_u32_e32 v245, v245, v50
	s_mov_b64 s[26:27], -1
	buffer_load_dword v226, v242, s[16:19], 0 offen sc1
	buffer_load_dword v227, v242, s[16:19], 0 offen offset:8 sc1
	buffer_load_dword v228, v242, s[16:19], 0 offen offset:16 sc1
	buffer_load_dword v229, v242, s[16:19], 0 offen offset:24 sc1
	buffer_load_dword v230, v243, s[16:19], 0 offen sc1
	buffer_load_dword v231, v243, s[16:19], 0 offen offset:8 sc1
	buffer_load_dword v232, v243, s[16:19], 0 offen offset:16 sc1
	buffer_load_dword v233, v243, s[16:19], 0 offen offset:24 sc1
	buffer_load_dword v234, v244, s[16:19], 0 offen sc1
	buffer_load_dword v235, v244, s[16:19], 0 offen offset:8 sc1
	buffer_load_dword v236, v244, s[16:19], 0 offen offset:16 sc1
	buffer_load_dword v237, v244, s[16:19], 0 offen offset:24 sc1
	buffer_load_dword v238, v245, s[16:19], 0 offen sc1
	buffer_load_dword v239, v245, s[16:19], 0 offen offset:8 sc1
	buffer_load_dword v240, v245, s[16:19], 0 offen offset:16 sc1
	buffer_load_dword v241, v245, s[16:19], 0 offen offset:24 sc1
.Lrec_step:
	s_bitcmp0_b32 s46, 2
	s_cselect_b32 s28, 0, s34
	s_cselect_b32 s47, s38, s31
	s_cselect_b32 s48, s40, s30
	s_mov_b32 s14, 0
.Lrec_w0:
	s_waitcnt vmcnt(3)
	v_bitop3_b32 v50, v226, v227, s28 bitop3:0x7e
	v_bitop3_b32 v51, v228, v229, s28 bitop3:0x7e
	v_bitop3_b32 v50, v50, v51, s34 bitop3:0xa8
	v_cmp_ne_u32_e32 vcc, 0, v50
	s_andn2_b64 vcc, vcc, s[26:27]
	s_cbranch_vccnz .Lrec_retry0
	s_cmp_eq_u32 s46, 0
	s_cbranch_scc1 .Lrec_norot
	v_accvgpr_read_b32 v43, a33
	v_accvgpr_read_b32 v42, a32
	v_accvgpr_write_b32 a33, v41
	v_accvgpr_write_b32 a32, v40
.Lrec_norot:
	s_nop 0
	v_fma_mix_f32 v246, v42, s40, v45 op_sel_hi:[1,0,0]
	v_fma_mix_f32 v247, v42, s40, v6 op_sel:[1,0,0] op_sel_hi:[1,0,0]
	v_fma_mix_f32 v248, v43, s38, v8 op_sel_hi:[1,0,0]
	v_fma_mix_f32 v249, v43, s40, v7 op_sel:[1,0,0] op_sel_hi:[1,0,0]
	v_smfmac_f32_16x16x64_f16 a[0:3], v[226:229], a[36:43], v26
	v_smfmac_f32_16x16x64_f16 a[4:7], v[226:229], a[68:75], v26
	v_smfmac_f32_16x16x64_f16 a[8:11], v[226:229], v[66:73], v26
	v_smfmac_f32_16x16x64_f16 a[12:15], v[226:229], v[98:105], v26
	v_smfmac_f32_16x16x64_f16 a[16:19], v[226:229], v[130:137], v26
	v_smfmac_f32_16x16x64_f16 a[20:23], v[226:229], v[162:169], v26
	v_smfmac_f32_16x16x64_f16 a[24:27], v[226:229], v[194:201], v26
	v_smfmac_f32_16x16x64_f16 a[28:31], v[226:229], a[120:127], v26
.Lrec_w1:
	s_waitcnt vmcnt(2)
	v_bitop3_b32 v50, v230, v231, s28 bitop3:0x7e
	v_bitop3_b32 v51, v232, v233, s28 bitop3:0x7e
	v_bitop3_b32 v50, v50, v51, s34 bitop3:0xa8
	v_cmp_ne_u32_e32 vcc, 0, v50
	s_andn2_b64 vcc, vcc, s[26:27]
	s_cbranch_vccnz .Lrec_retry1
	v_smfmac_f32_16x16x64_f16 a[0:3], v[230:233], a[44:51], v26
	v_smfmac_f32_16x16x64_f16 a[4:7], v[230:233], a[76:83], v26
	v_smfmac_f32_16x16x64_f16 a[8:11], v[230:233], v[74:81], v26
	v_smfmac_f32_16x16x64_f16 a[12:15], v[230:233], v[106:113], v26
	v_smfmac_f32_16x16x64_f16 a[16:19], v[230:233], v[138:145], v26
	v_smfmac_f32_16x16x64_f16 a[20:23], v[230:233], v[170:177], v26
	v_smfmac_f32_16x16x64_f16 a[24:27], v[230:233], v[202:209], v26
	v_smfmac_f32_16x16x64_f16 a[28:31], v[230:233], a[128:135], v26
.Lrec_w2:
	s_waitcnt vmcnt(1)
	v_bitop3_b32 v50, v234, v235, s28 bitop3:0x7e
	v_bitop3_b32 v51, v236, v237, s28 bitop3:0x7e
	v_bitop3_b32 v50, v50, v51, s34 bitop3:0xa8
	v_cmp_ne_u32_e32 vcc, 0, v50
	s_andn2_b64 vcc, vcc, s[26:27]
	s_cbranch_vccnz .Lrec_retry2
	v_smfmac_f32_16x16x64_f16 a[0:3], v[234:237], a[52:59], v26
	v_smfmac_f32_16x16x64_f16 a[4:7], v[234:237], a[84:91], v26
	v_smfmac_f32_16x16x64_f16 a[8:11], v[234:237], v[82:89], v26
	v_smfmac_f32_16x16x64_f16 a[12:15], v[234:237], v[114:121], v26
	v_smfmac_f32_16x16x64_f16 a[16:19], v[234:237], v[146:153], v26
	v_smfmac_f32_16x16x64_f16 a[20:23], v[234:237], v[178:185], v26
	v_smfmac_f32_16x16x64_f16 a[24:27], v[234:237], v[210:217], v26
	v_smfmac_f32_16x16x64_f16 a[28:31], v[234:237], a[136:143], v26
.Lrec_w3:
	s_waitcnt vmcnt(0)
	v_bitop3_b32 v50, v238, v239, s28 bitop3:0x7e
	v_bitop3_b32 v51, v240, v241, s28 bitop3:0x7e
	v_bitop3_b32 v50, v50, v51, s34 bitop3:0xa8
	v_cmp_ne_u32_e32 vcc, 0, v50
	s_andn2_b64 vcc, vcc, s[26:27]
	s_cbranch_vccnz .Lrec_retry3
	s_add_i32 s14, s46, 1
	s_lshl_b32 s6, s14, 13
	s_lshl_b32 s7, s14, 17
	s_and_b32 s6, s6, 0x8000
	s_and_b32 s7, s7, 0x60000
	v_add_u32_e32 v242, s7, v27
	v_add_u32_e32 v243, s7, v28
	v_add_u32_e32 v244, s7, v29
	v_add_u32_e32 v245, s7, v30
	v_smfmac_f32_16x16x64_f16 a[0:3], v[238:241], a[60:67], v26
	v_smfmac_f32_16x16x64_f16 a[4:7], v[238:241], v[58:65], v26
	v_smfmac_f32_16x16x64_f16 a[8:11], v[238:241], v[90:97], v26
	v_smfmac_f32_16x16x64_f16 a[12:15], v[238:241], v[122:129], v26
	v_smfmac_f32_16x16x64_f16 a[16:19], v[238:241], v[154:161], v26
	v_smfmac_f32_16x16x64_f16 a[20:23], v[238:241], v[186:193], v26
	v_smfmac_f32_16x16x64_f16 a[24:27], v[238:241], v[218:225], v26
	v_smfmac_f32_16x16x64_f16 a[28:31], v[238:241], a[112:119], v26
	s_nop 0
	ds_write_b32 v31, a0
	ds_write_b32 v32, a1
	ds_write_b32 v33, a2
	ds_write_b32 v34, a3
	ds_write_b32 v31, a4 offset:64
	ds_write_b32 v32, a5 offset:64
	ds_write_b32 v33, a6 offset:64
	ds_write_b32 v34, a7 offset:64
	ds_write_b32 v35, a8
	ds_write_b32 v36, a9
	ds_write_b32 v37, a10
	ds_write_b32 v38, a11
	ds_write_b32 v35, a12 offset:64
	ds_write_b32 v36, a13 offset:64
	ds_write_b32 v37, a14 offset:64
	ds_write_b32 v38, a15 offset:64
	ds_write_b32 v31, a16 offset:256
	ds_write_b32 v32, a17 offset:256
	ds_write_b32 v33, a18 offset:256
	ds_write_b32 v34, a19 offset:256
	ds_write_b32 v31, a20 offset:320
	ds_write_b32 v32, a21 offset:320
	ds_write_b32 v33, a22 offset:320
	ds_write_b32 v34, a23 offset:320
	ds_write_b32 v35, a24 offset:256
	ds_write_b32 v36, a25 offset:256
	ds_write_b32 v37, a26 offset:256
	ds_write_b32 v38, a27 offset:256
	ds_write_b32 v35, a28 offset:320
	ds_write_b32 v36, a29 offset:320
	ds_write_b32 v37, a30 offset:320
	ds_write_b32 v38, a31 offset:320
	s_waitcnt lgkmcnt(0)
	s_barrier
	ds_read_b128 v[10:13], v9
	ds_read_b128 v[14:17], v9 offset:4096
	ds_read_b128 v[18:21], v9 offset:8192
	ds_read_b128 v[22:25], v9 offset:12288
	ds_read_b128 v[46:49], v9 offset:16384
	ds_read_b128 v[50:53], v9 offset:20480
	ds_read_b128 v[2:5], v9 offset:24576
	ds_read_b128 v[250:253], v9 offset:28672
	s_min_u32 s29, s46, 0xfd
	s_lshl_b32 s29, s29, 19
	s_add_u32 s29, s29, s36
	v_mov_b32_e32 v54, s29
	v_add_co_u32_e32 v54, vcc, v254, v54
	s_nop 1
	v_addc_co_u32_e32 v55, vcc, 0, v255, vcc
	global_load_dwordx2 v[40:41], v[54:55], off
	s_waitcnt lgkmcnt(6)
	v_pk_add_f32 v[10:11], v[10:11], v[14:15]
	v_pk_add_f32 v[12:13], v[12:13], v[16:17]
	s_waitcnt lgkmcnt(4)
	v_pk_add_f32 v[18:19], v[18:19], v[22:23]
	v_pk_add_f32 v[20:21], v[20:21], v[24:25]
	s_waitcnt lgkmcnt(2)
	v_pk_add_f32 v[46:47], v[46:47], v[50:51]
	v_pk_add_f32 v[48:49], v[48:49], v[52:53]
	v_pk_add_f32 v[10:11], v[10:11], v[18:19]
	v_pk_add_f32 v[12:13], v[12:13], v[20:21]
	s_waitcnt lgkmcnt(0)
	v_pk_add_f32 v[2:3], v[2:3], v[250:251]
	v_pk_add_f32 v[4:5], v[4:5], v[252:253]
	v_pk_add_f32 v[46:47], v[46:47], v[2:3]
	v_pk_add_f32 v[48:49], v[48:49], v[4:5]
	v_pk_add_f32 v[10:11], v[10:11], v[46:47]
	v_pk_add_f32 v[12:13], v[12:13], v[48:49]
	v_fmac_f32_e32 v247, s48, v11
	v_fmac_f32_e32 v246, s48, v10
	v_fmac_f32_e32 v249, s48, v13
	v_fmac_f32_e32 v248, s47, v12
	v_exp_f32_e32 v15, v247
	v_exp_f32_e32 v14, v246
	v_exp_f32_e32 v17, v249
	v_max_f32_e32 v16, 0, v248
	v_add_f32_e32 v15, 1.0, v15
	v_add_f32_e32 v14, 1.0, v14
	v_add_f32_e32 v17, 1.0, v17
	v_rcp_f32_e32 v14, v14
	v_rcp_f32_e32 v15, v15
	v_rcp_f32_e32 v17, v17
	v_add_u32_e32 v18, s7, v1
	v_mul_f32_e32 v12, v16, v14
	v_fmac_f32_e32 v12, v44, v15
	v_max_f32_e32 v19, 0, v12
	v_mul_f32_e32 v13, v17, v19
	v_fma_mixlo_f16 v14, v13, s45, 0
	s_lshl_b32 s29, s46, 3
	v_and_b32_e32 v14, 0x7fff, v14
	s_andn2_b64 vcc, exec, s[4:5]
	v_or_b32_e32 v16, s6, v14
	s_cbranch_vccnz .Lrec_slowst
	buffer_store_short v16, v18, s[20:23], 0 offen
	s_branch .Lrec_stored

.Lrec_stored:
	s_cmpk_eq_i32 s14, 0x100
	s_cbranch_scc1 .Lrec_exit
	buffer_load_dwordx4 v[226:229], v242, s[20:23], 0 offen sc1
	buffer_load_dwordx4 v[230:233], v243, s[20:23], 0 offen sc1
	buffer_load_dwordx4 v[234:237], v244, s[20:23], 0 offen sc1
	buffer_load_dwordx4 v[238:241], v245, s[20:23], 0 offen sc1
	v_and_or_b32 v15, s29, 56, v56
	v_lshl_add_u32 v15, v15, 6, v0
	ds_write_b16 v15, v14 offset:33024
	v_mov_b32_e32 v44, v12
	v_accvgpr_write_b32 a0, 0
	v_accvgpr_write_b32 a1, 0
	v_accvgpr_write_b32 a2, 0
	v_accvgpr_write_b32 a3, 0
	v_accvgpr_write_b32 a4, 0
	v_accvgpr_write_b32 a5, 0
	v_accvgpr_write_b32 a6, 0
	v_accvgpr_write_b32 a7, 0
	v_accvgpr_write_b32 a8, 0
	v_accvgpr_write_b32 a9, 0
	v_accvgpr_write_b32 a10, 0
	v_accvgpr_write_b32 a11, 0
	v_accvgpr_write_b32 a12, 0
	v_accvgpr_write_b32 a13, 0
	v_accvgpr_write_b32 a14, 0
	v_accvgpr_write_b32 a15, 0
	v_accvgpr_write_b32 a16, 0
	v_accvgpr_write_b32 a17, 0
	v_accvgpr_write_b32 a18, 0
	v_accvgpr_write_b32 a19, 0
	v_accvgpr_write_b32 a20, 0
	v_accvgpr_write_b32 a21, 0
	v_accvgpr_write_b32 a22, 0
	v_accvgpr_write_b32 a23, 0
	v_accvgpr_write_b32 a24, 0
	v_accvgpr_write_b32 a25, 0
	v_accvgpr_write_b32 a26, 0
	v_accvgpr_write_b32 a27, 0
	v_accvgpr_write_b32 a28, 0
	v_accvgpr_write_b32 a29, 0
	v_accvgpr_write_b32 a30, 0
	v_accvgpr_write_b32 a31, 0
	v_xor_b32_e32 v31, 0x10000, v31
	v_xor_b32_e32 v32, 0x10000, v32
	v_xor_b32_e32 v33, 0x10000, v33
	v_xor_b32_e32 v34, 0x10000, v34
	v_xor_b32_e32 v35, 0x10000, v35
	v_xor_b32_e32 v36, 0x10000, v36
	v_xor_b32_e32 v37, 0x10000, v37
	v_xor_b32_e32 v38, 0x10000, v38
	v_xor_b32_e32 v9, 0x10000, v9
	s_mov_b64 s[26:27], s[24:25]
	s_cmp_eq_u64 s[2:3], 0
	s_cbranch_scc1 .Lrec_noflush
	s_and_b32 s29, s46, 3
	s_cmp_lg_u32 s29, 0
	s_cbranch_scc1 .Lrec_noflush
	s_cmp_lt_u32 s46, 4
	s_cbranch_scc1 .Lrec_noflush
	s_add_i32 s29, s46, -4
	v_accvgpr_read_b32 v46, a94
	v_or_b32_e32 v50, s29, v46
	v_lshlrev_b32_e32 v46, 3, v50
	v_accvgpr_read_b32 v47, a95
	v_and_or_b32 v46, v46, 40, v47
	v_accvgpr_read_b32 v47, a96
	v_lshl_add_u32 v47, v47, 1, 0
	v_lshl_add_u32 v54, v46, 6, v47
	ds_read_b128 v[46:49], v54 offset:33024
	v_ashrrev_i32_e32 v51, 31, v50
	v_accvgpr_read_b32 v52, a100
	v_lshlrev_b64 v[50:51], 17, v[50:51]
	v_accvgpr_read_b32 v53, a101
	v_lshl_add_u64 v[50:51], v[52:53], 0, v[50:51]
	v_add_co_u32_e32 v52, vcc, 0x20000, v50
	s_nop 1
	v_addc_co_u32_e32 v53, vcc, 0, v51, vcc
	s_waitcnt lgkmcnt(0)
	global_store_dwordx4 v[52:53], v[46:49], off
	s_nop 1
	ds_read_b128 v[46:49], v54 offset:34048
	v_add_co_u32_e32 v50, vcc, 0x60000, v50
	s_nop 1
	v_addc_co_u32_e32 v51, vcc, 0, v51, vcc
	s_waitcnt lgkmcnt(0)
	global_store_dwordx4 v[50:51], v[46:49], off
.Lrec_noflush:
	s_mov_b32 s46, s14
	s_branch .Lrec_step
.Lrec_exit:
	v_and_or_b32 v15, s29, 56, v56
	v_lshl_add_u32 v15, v15, 6, v0
	ds_write_b16 v15, v14 offset:33024
	s_branch .LBB5_40
.Lrec_retry0:
	s_add_i32 s14, s14, 1
	s_cmp_gt_u32 s14, 0x40000
	s_cbranch_scc1 .Lrec_dead0
	s_sleep 1
	buffer_load_dwordx4 v[226:229], v242, s[20:23], 0 offen sc1
	buffer_load_dwordx4 v[230:233], v243, s[20:23], 0 offen sc1
	buffer_load_dwordx4 v[234:237], v244, s[20:23], 0 offen sc1
	buffer_load_dwordx4 v[238:241], v245, s[20:23], 0 offen sc1
	s_branch .Lrec_w0

.Lrec_retry1:
	s_add_i32 s14, s14, 1
	s_cmp_gt_u32 s14, 0x40000
	s_cbranch_scc1 .Lrec_dead1
	s_sleep 1
	buffer_load_dwordx4 v[230:233], v243, s[20:23], 0 offen sc1
	buffer_load_dwordx4 v[234:237], v244, s[20:23], 0 offen sc1
	buffer_load_dwordx4 v[238:241], v245, s[20:23], 0 offen sc1
	s_branch .Lrec_w1

.Lrec_retry2:
	s_add_i32 s14, s14, 1
	s_cmp_gt_u32 s14, 0x40000
	s_cbranch_scc1 .Lrec_dead2
	s_sleep 1
	buffer_load_dwordx4 v[234:237], v244, s[20:23], 0 offen sc1
	buffer_load_dwordx4 v[238:241], v245, s[20:23], 0 offen sc1
	s_branch .Lrec_w2

.Lrec_retry3:
	s_add_i32 s14, s14, 1
	s_cmp_gt_u32 s14, 0x40000
	s_cbranch_scc1 .Lrec_dead3
	s_sleep 1
	buffer_load_dwordx4 v[238:241], v245, s[20:23], 0 offen sc1
	s_branch .Lrec_w3

	.amdhsa_kernel _Z5k_recPKDF16_S0_PKfS0_jjS2_PfS3_PDF16_Pj
		.amdhsa_group_segment_fixed_size 0
		.amdhsa_private_segment_fixed_size 0
		.amdhsa_kernarg_size 80
		.amdhsa_user_sgpr_count 2
		.amdhsa_user_sgpr_dispatch_ptr 0
		.amdhsa_user_sgpr_queue_ptr 0
		.amdhsa_user_sgpr_kernarg_segment_ptr 1
		.amdhsa_user_sgpr_dispatch_id 0
		.amdhsa_user_sgpr_kernarg_preload_length 0
		.amdhsa_user_sgpr_kernarg_preload_offset 0
		.amdhsa_user_sgpr_private_segment_size 0
		.amdhsa_uses_dynamic_stack 0
		.amdhsa_enable_private_segment 0
		.amdhsa_system_sgpr_workgroup_id_x 1
		.amdhsa_system_sgpr_workgroup_id_y 0
		.amdhsa_system_sgpr_workgroup_id_z 0
		.amdhsa_system_sgpr_workgroup_info 0
		.amdhsa_system_vgpr_workitem_id 0
		.amdhsa_next_free_vgpr 400
		.amdhsa_next_free_sgpr 50
		.amdhsa_accum_offset 256
		.amdhsa_reserve_vcc 1
		.amdhsa_float_round_mode_32 0
		.amdhsa_float_round_mode_16_64 0
		.amdhsa_float_denorm_mode_32 3
		.amdhsa_float_denorm_mode_16_64 3
		.amdhsa_dx10_clamp 1
		.amdhsa_ieee_mode 1
		.amdhsa_fp16_overflow 0
		.amdhsa_tg_split 0
		.amdhsa_exception_fp_ieee_invalid_op 0
		.amdhsa_exception_fp_denorm_src 0
		.amdhsa_exception_fp_ieee_div_zero 0
		.amdhsa_exception_fp_ieee_overflow 0
		.amdhsa_exception_fp_ieee_underflow 0
		.amdhsa_exception_fp_ieee_inexact 0
		.amdhsa_exception_int_div_zero 0
	.end_amdhsa_kernel

amdhsa.kernels:
  - .agpr_count:     0
    .args:
      - .offset:         0
        .size:           288
        .value_kind:     by_value
    .group_segment_fixed_size: 16640
    .kernarg_segment_align: 8
    .kernarg_segment_size: 288
    .language:       OpenCL C
    .language_version:
      - 2
      - 0
    .max_flat_workgroup_size: 1024
    .name:           _Z8k_wt_all6WtJobs
    .private_segment_fixed_size: 0
    .sgpr_count:     30
    .sgpr_spill_count: 0
    .symbol:         _Z8k_wt_all6WtJobs.kd
    .uniform_work_group_size: 1
    .uses_dynamic_stack: false
    .vgpr_count:     44
    .vgpr_spill_count: 0
    .wavefront_size: 64
  - .agpr_count:     0
    .args:
      - .actual_access:  read_only
        .address_space:  global
        .offset:         0
        .size:           8
        .value_kind:     global_buffer
      - .actual_access:  read_only
        .address_space:  global
        .offset:         8
        .size:           8
        .value_kind:     global_buffer
      - .actual_access:  write_only
        .address_space:  global
        .offset:         16
        .size:           8
        .value_kind:     global_buffer
    .group_segment_fixed_size: 0
    .kernarg_segment_align: 8
    .kernarg_segment_size: 24
    .language:       OpenCL C
    .language_version:
      - 2
      - 0
    .max_flat_workgroup_size: 1024
    .name:           _Z8k_prepA1PKfS0_PDF16_
    .private_segment_fixed_size: 0
    .sgpr_count:     16
    .sgpr_spill_count: 0
    .symbol:         _Z8k_prepA1PKfS0_PDF16_.kd
    .uniform_work_group_size: 1
    .uses_dynamic_stack: false
    .vgpr_count:     15
    .vgpr_spill_count: 0
    .wavefront_size: 64
  - .agpr_count:     0
    .args:
      - .actual_access:  read_only
        .address_space:  global
        .offset:         0
        .size:           8
        .value_kind:     global_buffer
      - .actual_access:  read_only
        .address_space:  global
        .offset:         8
        .size:           8
        .value_kind:     global_buffer
      - .actual_access:  read_only
        .address_space:  global
        .offset:         16
        .size:           8
        .value_kind:     global_buffer
      - .actual_access:  write_only
        .address_space:  global
        .offset:         24
        .size:           8
        .value_kind:     global_buffer
    .group_segment_fixed_size: 4096
    .kernarg_segment_align: 8
    .kernarg_segment_size: 32
    .language:       OpenCL C
    .language_version:
      - 2
      - 0
    .max_flat_workgroup_size: 1024
    .name:           _Z7k_bias0PKfPKiS0_Pf
    .private_segment_fixed_size: 0
    .sgpr_count:     28
    .sgpr_spill_count: 0
    .symbol:         _Z7k_bias0PKfPKiS0_Pf.kd
    .uniform_work_group_size: 1
    .uses_dynamic_stack: false
    .vgpr_count:     78
    .vgpr_spill_count: 0
    .wavefront_size: 64
  - .agpr_count:     0
    .args:
      - .actual_access:  read_only
        .address_space:  global
        .offset:         0
        .size:           8
        .value_kind:     global_buffer
      - .actual_access:  read_only
        .address_space:  global
        .offset:         8
        .size:           8
        .value_kind:     global_buffer
      - .actual_access:  read_only
        .address_space:  global
        .offset:         16
        .size:           8
        .value_kind:     global_buffer
      - .actual_access:  read_only
        .address_space:  global
        .offset:         24
        .size:           8
        .value_kind:     global_buffer
      - .actual_access:  read_only
        .address_space:  global
        .offset:         32
        .size:           8
        .value_kind:     global_buffer
      - .actual_access:  write_only
        .address_space:  global
        .offset:         40
        .size:           8
        .value_kind:     global_buffer
    .group_segment_fixed_size: 0
    .kernarg_segment_align: 8
    .kernarg_segment_size: 48
    .language:       OpenCL C
    .language_version:
      - 2
      - 0
    .max_flat_workgroup_size: 1024
    .name:           _Z7k_biasLPKfS0_S0_S0_S0_Pf
    .private_segment_fixed_size: 0
    .sgpr_count:     24
    .sgpr_spill_count: 0
    .symbol:         _Z7k_biasLPKfS0_S0_S0_S0_Pf.kd
    .uniform_work_group_size: 1
    .uses_dynamic_stack: false
    .vgpr_count:     29
    .vgpr_spill_count: 0
    .wavefront_size: 64
  - .agpr_count:     0
    .args:
      - .actual_access:  read_only
        .address_space:  global
        .offset:         0
        .size:           8
        .value_kind:     global_buffer
      - .actual_access:  read_only
        .address_space:  global
        .offset:         8
        .size:           8
        .value_kind:     global_buffer
      - .actual_access:  write_only
        .address_space:  global
        .offset:         16
        .size:           8
        .value_kind:     global_buffer
      - .actual_access:  write_only
        .address_space:  global
        .offset:         24
        .size:           8
        .value_kind:     global_buffer
    .group_segment_fixed_size: 0
    .kernarg_segment_align: 8
    .kernarg_segment_size: 32
    .language:       OpenCL C
    .language_version:
      - 2
      - 0
    .max_flat_workgroup_size: 1024
    .name:           _Z8k_state0PKfS0_PDF16_Pf
    .private_segment_fixed_size: 0
    .sgpr_count:     18
    .sgpr_spill_count: 0
    .symbol:         _Z8k_state0PKfS0_PDF16_Pf.kd
    .uniform_work_group_size: 1
    .uses_dynamic_stack: false
    .vgpr_count:     7
    .vgpr_spill_count: 0
    .wavefront_size: 64
  - .agpr_count:     144
    .args:
      - .actual_access:  read_only
        .address_space:  global
        .offset:         0
        .size:           8
        .value_kind:     global_buffer
      - .actual_access:  read_only
        .address_space:  global
        .offset:         8
        .size:           8
        .value_kind:     global_buffer
      - .actual_access:  read_only
        .address_space:  global
        .offset:         16
        .size:           8
        .value_kind:     global_buffer
      - .address_space:  global
        .offset:         24
        .size:           8
        .value_kind:     global_buffer
      - .offset:         32
        .size:           4
        .value_kind:     by_value
      - .offset:         36
        .size:           4
        .value_kind:     by_value
      - .address_space:  global
        .offset:         40
        .size:           8
        .value_kind:     global_buffer
      - .address_space:  global
        .offset:         48
        .size:           8
        .value_kind:     global_buffer
      - .address_space:  global
        .offset:         56
        .size:           8
        .value_kind:     global_buffer
      - .address_space:  global
        .offset:         64
        .size:           8
        .value_kind:     global_buffer
      - .address_space:  global
        .offset:         72
        .size:           8
        .value_kind:     global_buffer
    .group_segment_fixed_size: 0
    .kernarg_segment_align: 8
    .kernarg_segment_size: 80
    .language:       OpenCL C
    .language_version:
      - 2
      - 0
    .max_flat_workgroup_size: 256
    .name:           _Z5k_recPKDF16_S0_PKfS0_jjS2_PfS3_PDF16_Pj
    .private_segment_fixed_size: 0
    .sgpr_count:     56
    .sgpr_spill_count: 0
    .symbol:         _Z5k_recPKDF16_S0_PKfS0_jjS2_PfS3_PDF16_Pj.kd
    .uniform_work_group_size: 1
    .uses_dynamic_stack: false
    .vgpr_count:     400
    .vgpr_spill_count: 0
    .wavefront_size: 64
  - .agpr_count:     0
    .args:
      - .address_space:  global
        .offset:         0
        .size:           8
        .value_kind:     global_buffer
    .group_segment_fixed_size: 0
    .kernarg_segment_align: 8
    .kernarg_segment_size: 8
    .language:       OpenCL C
    .language_version:
      - 2
      - 0
    .max_flat_workgroup_size: 1024
    .name:           _Z9k_softmaxPf
    .private_segment_fixed_size: 0
    .sgpr_count:     9
    .sgpr_spill_count: 0
    .symbol:         _Z9k_softmaxPf.kd
    .uniform_work_group_size: 1
    .uses_dynamic_stack: false
    .vgpr_count:     32
    .vgpr_spill_count: 0
    .wavefront_size: 64
  - .agpr_count:     0
    .args:
      - .address_space:  global
        .offset:         0
        .size:           8
        .value_kind:     global_buffer
      - .address_space:  global
        .offset:         8
        .size:           8
        .value_kind:     global_buffer
      - .actual_access:  write_only
        .address_space:  global
        .offset:         16
        .size:           8
        .value_kind:     global_buffer
      - .actual_access:  read_only
        .address_space:  global
        .offset:         24
        .size:           8
        .value_kind:     global_buffer
    .group_segment_fixed_size: 0
    .kernarg_segment_align: 8
    .kernarg_segment_size: 32
    .language:       OpenCL C
    .language_version:
      - 2
      - 0
    .max_flat_workgroup_size: 512
    .name:           _Z6k_gemmILi16384ELi4096ELi2048ELi0EEvPKDF16_S1_PvPKf
    .private_segment_fixed_size: 0
    .sgpr_count:     25
    .sgpr_spill_count: 0
    .symbol:         _Z6k_gemmILi16384ELi4096ELi2048ELi0EEvPKDF16_S1_PvPKf.kd
    .uniform_work_group_size: 1
    .uses_dynamic_stack: false
    .vgpr_count:     244
    .vgpr_spill_count: 0
    .wavefront_size: 64
  - .agpr_count:     0
    .args:
      - .address_space:  global
        .offset:         0
        .size:           8
        .value_kind:     global_buffer
      - .address_space:  global
        .offset:         8
        .size:           8
        .value_kind:     global_buffer
      - .actual_access:  write_only
        .address_space:  global
        .offset:         16
        .size:           8
        .value_kind:     global_buffer
      - .actual_access:  read_only
        .address_space:  global
        .offset:         24
        .size:           8
        .value_kind:     global_buffer
    .group_segment_fixed_size: 0
    .kernarg_segment_align: 8
    .kernarg_segment_size: 32
    .language:       OpenCL C
    .language_version:
      - 2
      - 0
    .max_flat_workgroup_size: 512
    .name:           _Z6k_gemmILi16384ELi4096ELi1024ELi0EEvPKDF16_S1_PvPKf
    .private_segment_fixed_size: 0
    .sgpr_count:     26
    .sgpr_spill_count: 0
    .symbol:         _Z6k_gemmILi16384ELi4096ELi1024ELi0EEvPKDF16_S1_PvPKf.kd
    .uniform_work_group_size: 1
    .uses_dynamic_stack: false
    .vgpr_count:     244
    .vgpr_spill_count: 0
    .wavefront_size: 64
  - .agpr_count:     0
    .args:
      - .address_space:  global
        .offset:         0
        .size:           8
        .value_kind:     global_buffer
      - .address_space:  global
        .offset:         8
        .size:           8
        .value_kind:     global_buffer
      - .actual_access:  write_only
        .address_space:  global
        .offset:         16
        .size:           8
        .value_kind:     global_buffer
      - .actual_access:  read_only
        .address_space:  global
        .offset:         24
        .size:           8
        .value_kind:     global_buffer
    .group_segment_fixed_size: 0
    .kernarg_segment_align: 8
    .kernarg_segment_size: 32
    .language:       OpenCL C
    .language_version:
      - 2
      - 0
    .max_flat_workgroup_size: 512
    .name:           _Z6k_gemmILi16384ELi1024ELi1024ELi1EEvPKDF16_S1_PvPKf
    .private_segment_fixed_size: 0
    .sgpr_count:     28
    .sgpr_spill_count: 0
    .symbol:         _Z6k_gemmILi16384ELi1024ELi1024ELi1EEvPKDF16_S1_PvPKf.kd
    .uniform_work_group_size: 1
    .uses_dynamic_stack: false
    .vgpr_count:     246
    .vgpr_spill_count: 0
    .wavefront_size: 64
